# attention softmax max: canonicalising v_max x,x pairs folded into the 2-input max (10 fewer VALU per step, wait-state distances kept with s_nop); on top of v26
# speedup vs baseline: 1.0011x; 1.0011x over previous
.LBB0_736:
	s_waitcnt vmcnt(8)
	ds_read_b128 v[14:17], v198
	ds_read_b128 v[18:21], v199
	ds_read_b128 v[22:25], v198 offset:2048
	ds_read_b128 v[26:29], v199 offset:2048
	ds_read_b128 v[30:33], v198 offset:32768
	ds_read_b128 v[34:37], v199 offset:32768
	ds_read_b128 v[38:41], v198 offset:34816
	ds_read_b128 v[42:45], v199 offset:34816
	s_waitcnt lgkmcnt(0)
	s_lshl_b32 m0, s96, 12
	s_add_u32 m0, m0, 0x10000
	s_nop 0
	global_load_lds_dwordx4 v118, s[100:101]
	s_add_u32 m0, m0, 0x400
	s_nop 0
	global_load_lds_dwordx4 v119, s[100:101]
	s_add_u32 m0, m0, 0x400
	s_nop 0
	global_load_lds_dwordx4 v120, s[100:101]
	s_add_u32 m0, m0, 0x400
	s_nop 0
	global_load_lds_dwordx4 v121, s[100:101]
	s_add_u32 m0, m0, 0x7400
	s_nop 0
	global_load_lds_dwordx4 v122, s[100:101]
	s_add_u32 m0, m0, 0x400
	s_nop 0
	global_load_lds_dwordx4 v123, s[100:101]
	s_add_u32 m0, m0, 0x400
	s_nop 0
	global_load_lds_dwordx4 v124, s[100:101]
	s_add_u32 m0, m0, 0x400
	s_nop 0
	global_load_lds_dwordx4 v125, s[100:101]
	s_waitcnt vmcnt(31)
	v_mfma_f32_16x16x32_bf16 v[170:173], v[14:17], v[6:9], v[170:173]
	s_mov_b32 s12, 0x40c00000
	s_waitcnt vmcnt(30)
	v_mfma_f32_16x16x32_bf16 v[182:185], v[18:21], v[10:13], v[170:173]
	s_waitcnt vmcnt(29)
	v_mfma_f32_16x16x32_bf16 v[170:173], v[22:25], v[6:9], v[174:177]
	s_waitcnt vmcnt(28)
	v_mfma_f32_16x16x32_bf16 v[178:181], v[26:29], v[10:13], v[170:173]
	s_nop 3
	s_nop 0
	s_nop 0
	v_max_f32_e32 v0, v184, v185
	s_waitcnt vmcnt(27)
	v_mfma_f32_16x16x32_bf16 v[170:173], v[30:33], v[6:9], v[186:189]
	v_max3_f32 v0, v182, v183, v0
	s_nop 0
	s_waitcnt vmcnt(26)
	v_mfma_f32_16x16x32_bf16 v[174:177], v[34:37], v[10:13], v[170:173]
	s_nop 0
	v_max_f32_e32 v153, v180, v181
	v_max3_f32 v153, v178, v179, v153
	s_waitcnt vmcnt(25) lgkmcnt(0)
	v_mfma_f32_16x16x32_bf16 v[170:173], v[38:41], v[6:9], v[190:193]
	s_waitcnt vmcnt(24)
	v_mfma_f32_16x16x32_bf16 v[170:173], v[42:45], v[10:13], v[170:173]
	s_nop 0
	s_nop 0
	s_nop 0
	v_max_f32_e32 v186, v174, v175
	s_nop 0
	s_nop 0
	v_max_f32_e32 v187, v176, v177
	s_nop 0
	v_max_f32_e32 v188, v173, v173
	v_max_f32_e32 v189, v172, v172
	v_max_f32_e32 v188, v189, v188
	v_max3_f32 v188, v170, v171, v188
	v_max3_f32 v186, v186, v187, v188
	v_max3_f32 v0, v0, v153, v186
	v_mov_b32_e32 v153, v0
	s_nop 1
	v_permlane16_swap_b32_e32 v0, v153
	s_nop 0
	s_nop 0
	v_max_f32_e32 v0, v0, v153
	v_mov_b32_e32 v153, v0
	s_nop 1
	v_permlane32_swap_b32_e32 v0, v153
	s_nop 0
	s_nop 0
	v_max_f32_e32 v0, v0, v153
	v_sub_f32_e32 v153, v0, v202
	v_mul_f32_e32 v153, 0x3e38aa3b, v153
	v_cmp_lt_f32_e32 vcc, s12, v153
	s_cbranch_vccz .LBB0_738
	v_max_f32_e32 v0, v0, v0
	v_max_f32_e32 v153, v202, v202
	v_max_f32_e32 v153, v153, v0
	v_sub_f32_e32 v0, v202, v153
	v_mul_f32_e32 v0, 0x3e38aa3b, v0
	v_exp_f32_e32 v0, v0
	v_mov_b32_e32 v202, v153
	v_pk_mul_f32 v[168:169], v[168:169], v[0:1] op_sel_hi:[1,0]
	v_pk_mul_f32 v[166:167], v[166:167], v[0:1] op_sel_hi:[1,0]
	v_pk_mul_f32 v[164:165], v[164:165], v[0:1] op_sel_hi:[1,0]
	v_pk_mul_f32 v[162:163], v[162:163], v[0:1] op_sel_hi:[1,0]
	v_pk_mul_f32 v[160:161], v[160:161], v[0:1] op_sel_hi:[1,0]
	v_pk_mul_f32 v[158:159], v[158:159], v[0:1] op_sel_hi:[1,0]
	v_pk_mul_f32 v[156:157], v[156:157], v[0:1] op_sel_hi:[1,0]
	v_pk_mul_f32 v[154:155], v[154:155], v[0:1] op_sel_hi:[1,0]
	v_mul_f32_e32 v244, v244, v0

.LBB0_760:
	s_waitcnt vmcnt(8)
	ds_read_b128 v[138:141], v198
	ds_read_b128 v[142:145], v199
	ds_read_b128 v[146:149], v198 offset:2048
	ds_read_b128 v[134:137], v199 offset:2048
	ds_read_b128 v[130:133], v198 offset:32768
	ds_read_b128 v[126:129], v199 offset:32768
	ds_read_b128 v[122:125], v198 offset:34816
	ds_read_b128 v[118:121], v199 offset:34816
	s_waitcnt lgkmcnt(0)
	s_lshl_b32 m0, s96, 12
	s_add_u32 m0, m0, 0x10000
	s_nop 0
	global_load_lds_dwordx4 v14, s[100:101]
	s_add_u32 m0, m0, 0x400
	s_nop 0
	global_load_lds_dwordx4 v15, s[100:101]
	s_add_u32 m0, m0, 0x400
	s_nop 0
	global_load_lds_dwordx4 v16, s[100:101]
	s_add_u32 m0, m0, 0x400
	s_nop 0
	global_load_lds_dwordx4 v17, s[100:101]
	s_add_u32 m0, m0, 0x7400
	s_nop 0
	global_load_lds_dwordx4 v18, s[100:101]
	s_add_u32 m0, m0, 0x400
	s_nop 0
	global_load_lds_dwordx4 v19, s[100:101]
	s_add_u32 m0, m0, 0x400
	s_nop 0
	global_load_lds_dwordx4 v20, s[100:101]
	s_add_u32 m0, m0, 0x400
	s_nop 0
	global_load_lds_dwordx4 v21, s[100:101]
	s_waitcnt vmcnt(31)
	v_mfma_f32_16x16x32_bf16 v[138:141], v[138:141], v[6:9], v[150:153]
	v_add_f32_e32 v0, v182, v183
	s_mov_b32 s12, 0x40c00000
	s_waitcnt vmcnt(27)
	v_mfma_f32_16x16x32_bf16 v[130:133], v[130:133], v[6:9], v[174:177]
	s_waitcnt vmcnt(25) lgkmcnt(0)
	v_mfma_f32_16x16x32_bf16 v[122:125], v[122:125], v[6:9], v[178:181]
	v_mfma_f32_16x16x32_bf16 v[138:141], v[142:145], v[10:13], v[138:141]
	v_add_f32_e32 v142, v244, v0
	v_mfma_f32_16x16x32_bf16 v[144:147], v[146:149], v[6:9], v[170:173]
	v_mfma_f32_16x16x32_bf16 v[126:129], v[126:129], v[10:13], v[130:133]
	s_nop 4
	s_nop 0
	s_nop 0
	v_max_f32_e32 v0, v140, v141
	s_waitcnt vmcnt(24)
	v_mfma_f32_16x16x32_bf16 v[118:121], v[118:121], v[10:13], v[122:125]
	v_max3_f32 v0, v138, v139, v0
	s_nop 0
	s_nop 0
	v_mfma_f32_16x16x32_bf16 v[134:137], v[134:137], v[10:13], v[144:147]
	v_max_f32_e32 v130, v126, v127
	s_nop 2
	v_max_f32_e32 v122, v121, v121
	v_max_f32_e32 v123, v120, v120
	v_max_f32_e32 v131, v129, v129
	v_max_f32_e32 v132, v128, v128
	v_max_f32_e32 v143, v137, v137
	v_max_f32_e32 v144, v136, v136
	v_max_f32_e32 v122, v123, v122
	v_max_f32_e32 v143, v144, v143
	v_max_f32_e32 v131, v132, v131
	v_max3_f32 v122, v118, v119, v122
	v_max3_f32 v143, v134, v135, v143
	v_max3_f32 v122, v130, v131, v122
	v_max3_f32 v0, v0, v143, v122
	v_mov_b32_e32 v122, v0
	s_nop 1
	v_permlane16_swap_b32_e32 v0, v122
	s_nop 0
	s_nop 0
	v_max_f32_e32 v0, v0, v122
	v_mov_b32_e32 v122, v0
	s_nop 1
	v_permlane32_swap_b32_e32 v0, v122
	s_nop 0
	s_nop 0
	v_max_f32_e32 v0, v0, v122
	v_sub_f32_e32 v122, v0, v202
	v_mul_f32_e32 v122, 0x3e38aa3b, v122
	v_cmp_lt_f32_e32 vcc, s12, v122
	s_cbranch_vccz .LBB0_762
	v_max_f32_e32 v0, v0, v0
	v_max_f32_e32 v122, v202, v202
	v_max_f32_e32 v143, v122, v0
	v_sub_f32_e32 v0, v202, v143
	v_mul_f32_e32 v0, 0x3e38aa3b, v0
	v_exp_f32_e32 v202, v0
	s_nop 0
	v_pk_mul_f32 v[186:187], v[142:143], v[202:203]
	v_pk_mul_f32 v[156:157], v[156:157], v[202:203] op_sel_hi:[1,0]
	v_pk_mul_f32 v[154:155], v[154:155], v[202:203] op_sel_hi:[1,0]
	v_pk_mul_f32 v[160:161], v[160:161], v[202:203] op_sel_hi:[1,0]
	v_pk_mul_f32 v[158:159], v[158:159], v[202:203] op_sel_hi:[1,0]
	v_pk_mul_f32 v[164:165], v[164:165], v[202:203] op_sel_hi:[1,0]
	v_pk_mul_f32 v[162:163], v[162:163], v[202:203] op_sel_hi:[1,0]
	v_pk_mul_f32 v[168:169], v[168:169], v[202:203] op_sel_hi:[1,0]
	v_pk_mul_f32 v[166:167], v[166:167], v[202:203] op_sel_hi:[1,0]
	v_mov_b32_e32 v202, v143
	v_mov_b32_e32 v142, v186
